# grid barrier spin loops: poll back-off s_sleep 1 -> 4 (fewer polling requests while the last workgroups finish)
# speedup vs baseline: 1.0053x; 1.0053x over previous
; __device__ __forceinline__ unsigned xb_ld(unsigned* p)              { return __hip_atomic_load(p, __ATOMIC_RELAXED, __HIP_MEMORY_SCOPE_AGENT); }
; __device__ __forceinline__ void xcd_barrier_complete(unsigned* bar, unsigned x, unsigned& nloc, unsigned& nx) {
;     const unsigned G = gridDim.x * gridDim.y * gridDim.z;
;     unsigned sum, cnt, mine, sp = 0u;
;     for (;;) {
;         sum = 0u; cnt = 0u; mine = 0u;
; #pragma unroll
;         for (unsigned j = 0; j < 16; ++j) { const unsigned c = xb_ld(&bar[XB_XCNT(j)]); sum += c; cnt += (c > 0u) ? 1u : 0u; }
;         mine = xb_ld(&bar[XB_XCNT(x)]);
;         if (sum == G) break;
;         __builtin_amdgcn_s_sleep(1);
;         if ((++sp & 255u) == 0u) { if (xb_ld(&bar[XB_TMO])) break; if (sp > XB_SPIN_CAP) { atomicAdd(&bar[XB_TMO], 1u); break; } }
;     }
.LBB0_56:
	v_mov_b64_e32 v[14:15], s[2:3]
	flat_load_dword v12, v[14:15] offset:1024 sc1
	flat_load_dword v1, v[14:15] offset:1280 sc1
	flat_load_dword v2, v[14:15] offset:1536 sc1
	flat_load_dword v3, v[14:15] offset:1792 sc1
	flat_load_dword v4, v[14:15] offset:2048 sc1
	flat_load_dword v5, v[14:15] offset:2304 sc1
	flat_load_dword v6, v[14:15] offset:2560 sc1
	flat_load_dword v7, v[14:15] offset:2816 sc1
	flat_load_dword v8, v[14:15] offset:3072 sc1
	flat_load_dword v9, v[14:15] offset:3328 sc1
	flat_load_dword v10, v[14:15] offset:3584 sc1
	flat_load_dword v11, v[14:15] offset:3840 sc1
	v_mov_b64_e32 v[14:15], s[6:7]
	flat_load_dword v13, v[14:15] sc1
	v_mov_b64_e32 v[14:15], s[8:9]
	flat_load_dword v14, v[14:15] sc1
	v_mov_b64_e32 v[16:17], s[10:11]
	flat_load_dword v15, v[16:17] sc1
	v_mov_b64_e32 v[16:17], s[12:13]
	flat_load_dword v16, v[16:17] sc1
	v_mov_b64_e32 v[18:19], s[4:5]
	flat_load_dword v17, v[18:19] sc1
	s_or_b64 s[20:21], s[20:21], exec
	s_or_b64 s[18:19], s[18:19], exec
	s_waitcnt vmcnt(0) lgkmcnt(0)
	v_add_u32_e32 v18, v1, v12
	v_add_u32_e32 v18, v18, v2
	v_add_u32_e32 v18, v18, v3
	v_add_u32_e32 v18, v18, v4
	v_add_u32_e32 v18, v18, v5
	v_add_u32_e32 v18, v18, v6
	v_add_u32_e32 v18, v18, v7
	v_add_u32_e32 v18, v18, v8
	v_add_u32_e32 v18, v18, v9
	v_add_u32_e32 v18, v18, v10
	v_add_u32_e32 v18, v18, v11
	v_add_u32_e32 v18, v18, v13
	v_add_u32_e32 v18, v18, v14
	v_add_u32_e32 v18, v18, v15
	v_add_u32_e32 v18, v18, v16
	v_cmp_ne_u32_e32 vcc, s34, v18
	s_and_saveexec_b64 s[22:23], vcc
	s_cbranch_execz .LBB0_55
	s_and_b32 s26, s35, 0xff
	s_mov_b64 s[24:25], -1
	s_cmp_eq_u32 s26, 0
	s_mov_b64 s[28:29], -1
	s_mov_b64 s[26:27], -1
	s_sleep 4
	s_cbranch_scc1 .LBB0_59
	s_and_saveexec_b64 s[30:31], s[28:29]
	s_cbranch_execz .LBB0_54
	s_branch .LBB0_62

.LBB0_70:
	s_and_b32 s18, s24, 0xff
	s_mov_b64 s[16:17], -1
	s_cmp_lg_u32 s18, 0
	s_mov_b64 s[18:19], -1
	s_sleep 4
	s_cbranch_scc1 .LBB0_74
	v_mov_b64_e32 v[2:3], s[2:3]
	flat_load_dword v2, v[2:3] offset:512 sc1
	s_mov_b64 s[18:19], 0
	s_mov_b64 s[20:21], -1
	s_waitcnt vmcnt(0) lgkmcnt(0)
	v_cmp_eq_u32_e32 vcc, 0, v2
	s_and_saveexec_b64 s[22:23], vcc
	s_cmp_lt_u32 s24, 0x400001
	s_cselect_b64 s[18:19], -1, 0
	s_xor_b64 s[20:21], exec, -1
	s_and_b64 s[18:19], s[18:19], exec
	s_or_b64 exec, exec, s[22:23]

.LBB0_84:
	s_and_b32 s18, s24, 0xff
	s_mov_b64 s[16:17], -1
	s_cmp_lg_u32 s18, 0
	s_mov_b64 s[20:21], -1
	s_sleep 4
	s_cbranch_scc0 .LBB0_86
	s_and_saveexec_b64 s[22:23], s[20:21]
	s_cbranch_execz .LBB0_83
	s_branch .LBB0_89

; __device__ __forceinline__ unsigned xb_ld(unsigned* p)              { return __hip_atomic_load(p, __ATOMIC_RELAXED, __HIP_MEMORY_SCOPE_AGENT); }
; __device__ __forceinline__ void xcd_barrier_complete(unsigned* bar, unsigned x, unsigned& nloc, unsigned& nx) {
;     const unsigned G = gridDim.x * gridDim.y * gridDim.z;
;     unsigned sum, cnt, mine, sp = 0u;
;     for (;;) {
;         sum = 0u; cnt = 0u; mine = 0u;
; #pragma unroll
;         for (unsigned j = 0; j < 16; ++j) { const unsigned c = xb_ld(&bar[XB_XCNT(j)]); sum += c; cnt += (c > 0u) ? 1u : 0u; }
;         mine = xb_ld(&bar[XB_XCNT(x)]);
;         if (sum == G) break;
;         __builtin_amdgcn_s_sleep(1);
;         if ((++sp & 255u) == 0u) { if (xb_ld(&bar[XB_TMO])) break; if (sp > XB_SPIN_CAP) { atomicAdd(&bar[XB_TMO], 1u); break; } }
;     }
.LBB0_129:
	v_mov_b64_e32 v[12:13], s[2:3]
	flat_load_dword v2, v[12:13] offset:1024 sc1
	flat_load_dword v1, v[12:13] offset:1280 sc1
	flat_load_dword v3, v[12:13] offset:1536 sc1
	s_or_b64 s[20:21], s[20:21], exec
	s_or_b64 s[18:19], s[18:19], exec
	s_waitcnt vmcnt(0) lgkmcnt(0)
	v_add_u32_e32 v4, v1, v2
	v_add_u32_e32 v5, v4, v3
	flat_load_dword v4, v[12:13] offset:1792 sc1
	s_waitcnt vmcnt(0) lgkmcnt(0)
	v_add_u32_e32 v6, v5, v4
	flat_load_dword v5, v[12:13] offset:2048 sc1
	s_waitcnt vmcnt(0) lgkmcnt(0)
	v_add_u32_e32 v7, v6, v5
	flat_load_dword v6, v[12:13] offset:2304 sc1
	s_waitcnt vmcnt(0) lgkmcnt(0)
	v_add_u32_e32 v8, v7, v6
	flat_load_dword v7, v[12:13] offset:2560 sc1
	s_waitcnt vmcnt(0) lgkmcnt(0)
	v_add_u32_e32 v9, v8, v7
	flat_load_dword v8, v[12:13] offset:2816 sc1
	s_waitcnt vmcnt(0) lgkmcnt(0)
	v_add_u32_e32 v10, v9, v8
	flat_load_dword v9, v[12:13] offset:3072 sc1
	s_waitcnt vmcnt(0) lgkmcnt(0)
	v_add_u32_e32 v11, v10, v9
	flat_load_dword v10, v[12:13] offset:3328 sc1
	s_waitcnt vmcnt(0) lgkmcnt(0)
	v_add_u32_e32 v14, v11, v10
	flat_load_dword v11, v[12:13] offset:3584 sc1
	s_waitcnt vmcnt(0) lgkmcnt(0)
	v_add_u32_e32 v14, v14, v11
	flat_load_dword v12, v[12:13] offset:3840 sc1
	s_waitcnt vmcnt(0) lgkmcnt(0)
	v_add_u32_e32 v16, v14, v12
	v_mov_b64_e32 v[14:15], s[6:7]
	flat_load_dword v13, v[14:15] sc1
	v_mov_b64_e32 v[14:15], s[8:9]
	flat_load_dword v14, v[14:15] sc1
	s_waitcnt vmcnt(0) lgkmcnt(0)
	v_add_u32_e32 v16, v16, v13
	v_add_u32_e32 v18, v16, v14
	v_mov_b64_e32 v[16:17], s[10:11]
	flat_load_dword v15, v[16:17] sc1
	v_mov_b64_e32 v[16:17], s[12:13]
	flat_load_dword v16, v[16:17] sc1
	s_waitcnt vmcnt(0) lgkmcnt(0)
	v_add_u32_e32 v18, v18, v15
	v_add_u32_e32 v20, v18, v16
	v_mov_b64_e32 v[18:19], s[4:5]
	flat_load_dword v17, v[18:19] sc1
	v_cmp_ne_u32_e32 vcc, s34, v20
	s_and_saveexec_b64 s[22:23], vcc
	s_cbranch_execz .LBB0_128
	s_and_b32 s26, s35, 0xff
	s_mov_b64 s[24:25], -1
	s_cmp_eq_u32 s26, 0
	s_mov_b64 s[28:29], -1
	s_mov_b64 s[26:27], -1
	s_sleep 4
	s_cbranch_scc1 .LBB0_132
	s_and_saveexec_b64 s[30:31], s[28:29]
	s_cbranch_execz .LBB0_127
	s_branch .LBB0_135

.LBB0_973:
	s_and_b32 s18, s24, 0xff
	s_mov_b64 s[16:17], -1
	s_cmp_lg_u32 s18, 0
	s_mov_b64 s[20:21], -1
	s_sleep 4
	s_cbranch_scc1 .LBB0_977
	v_mov_b64_e32 v[2:3], s[8:9]
	flat_load_dword v2, v[2:3] sc1
	s_mov_b64 s[20:21], 0
	s_mov_b64 s[18:19], -1
	s_waitcnt vmcnt(0) lgkmcnt(0)
	v_cmp_eq_u32_e32 vcc, 0, v2
	s_and_saveexec_b64 s[22:23], vcc
	s_cmp_lt_u32 s24, 0x400001
	s_cselect_b64 s[20:21], -1, 0
	s_xor_b64 s[18:19], exec, -1
	s_and_b64 s[20:21], s[20:21], exec
	s_or_b64 exec, exec, s[22:23]

; __device__ __forceinline__ unsigned xb_ld(unsigned* p)              { return __hip_atomic_load(p, __ATOMIC_RELAXED, __HIP_MEMORY_SCOPE_AGENT); }
; __device__ __forceinline__ void xcd_barrier_complete(unsigned* bar, unsigned x, unsigned& nloc, unsigned& nx) {
;     const unsigned G = gridDim.x * gridDim.y * gridDim.z;
;     unsigned sum, cnt, mine, sp = 0u;
;     for (;;) {
;         sum = 0u; cnt = 0u; mine = 0u;
; #pragma unroll
;         for (unsigned j = 0; j < 16; ++j) { const unsigned c = xb_ld(&bar[XB_XCNT(j)]); sum += c; cnt += (c > 0u) ? 1u : 0u; }
;         mine = xb_ld(&bar[XB_XCNT(x)]);
;         if (sum == G) break;
;         __builtin_amdgcn_s_sleep(1);
;         if ((++sp & 255u) == 0u) { if (xb_ld(&bar[XB_TMO])) break; if (sp > XB_SPIN_CAP) { atomicAdd(&bar[XB_TMO], 1u); break; } }
;     }
.LBB0_1406:
	flat_load_dword v28, v[0:1] offset:1024 sc1
	flat_load_dword v12, v[0:1] offset:1280 sc1
	flat_load_dword v13, v[0:1] offset:1536 sc1
	flat_load_dword v14, v[0:1] offset:1792 sc1
	flat_load_dword v15, v[0:1] offset:2048 sc1
	flat_load_dword v16, v[0:1] offset:2304 sc1
	flat_load_dword v17, v[0:1] offset:2560 sc1
	flat_load_dword v18, v[0:1] offset:2816 sc1
	flat_load_dword v19, v[0:1] offset:3072 sc1
	flat_load_dword v20, v[0:1] offset:3328 sc1
	flat_load_dword v21, v[0:1] offset:3584 sc1
	flat_load_dword v22, v[0:1] offset:3840 sc1
	flat_load_dword v23, v[2:3] sc1
	flat_load_dword v24, v[4:5] sc1
	flat_load_dword v25, v[6:7] sc1
	flat_load_dword v26, v[8:9] sc1
	flat_load_dword v27, v[10:11] sc1
	s_or_b64 s[10:11], s[10:11], exec
	s_or_b64 s[8:9], s[8:9], exec
	s_waitcnt vmcnt(0) lgkmcnt(0)
	v_add_u32_e32 v29, v12, v28
	v_add_u32_e32 v29, v29, v13
	v_add_u32_e32 v29, v29, v14
	v_add_u32_e32 v29, v29, v15
	v_add_u32_e32 v29, v29, v16
	v_add_u32_e32 v29, v29, v17
	v_add_u32_e32 v29, v29, v18
	v_add_u32_e32 v29, v29, v19
	v_add_u32_e32 v29, v29, v20
	v_add_u32_e32 v29, v29, v21
	v_add_u32_e32 v29, v29, v22
	v_add_u32_e32 v29, v29, v23
	v_add_u32_e32 v29, v29, v24
	v_add_u32_e32 v29, v29, v25
	v_add_u32_e32 v29, v29, v26
	v_cmp_ne_u32_e32 vcc, s23, v29
	s_and_saveexec_b64 s[12:13], vcc
	s_cbranch_execz .LBB0_1405
	s_and_b32 s16, s22, 0xff
	s_mov_b64 s[14:15], -1
	s_cmp_eq_u32 s16, 0
	s_mov_b64 s[18:19], -1
	s_mov_b64 s[16:17], -1
	s_sleep 4
	s_cbranch_scc0 .LBB0_1411
	flat_load_dword v29, v[0:1] offset:512 sc1
	s_mov_b64 s[18:19], 0
	s_waitcnt vmcnt(0) lgkmcnt(0)
	v_cmp_eq_u32_e32 vcc, 0, v29
	s_and_saveexec_b64 s[20:21], vcc
	s_cmp_lt_u32 s22, 0x400001
	s_cselect_b64 s[18:19], -1, 0
	s_xor_b64 s[16:17], exec, -1
	s_and_b64 s[18:19], s[18:19], exec
	s_or_b64 exec, exec, s[20:21]

.LBB0_1420:
	s_and_b32 s18, s25, 0xff
	s_mov_b64 s[16:17], -1
	s_cmp_lg_u32 s18, 0
	s_mov_b64 s[18:19], -1
	s_sleep 4
	s_cbranch_scc1 .LBB0_1424
	v_mov_b64_e32 v[2:3], s[2:3]
	flat_load_dword v0, v[2:3] offset:512 sc1
	s_mov_b64 s[18:19], 0
	s_mov_b64 s[20:21], -1
	s_waitcnt vmcnt(0) lgkmcnt(0)
	v_cmp_eq_u32_e32 vcc, 0, v0
	s_and_saveexec_b64 s[22:23], vcc
	s_cmp_lt_u32 s25, 0x400001
	s_cselect_b64 s[18:19], -1, 0
	s_xor_b64 s[20:21], exec, -1
	s_and_b64 s[18:19], s[18:19], exec
	s_or_b64 exec, exec, s[22:23]

.LBB0_1434:
	s_and_b32 s16, s25, 0xff
	s_cmp_lg_u32 s16, 0
	s_mov_b64 s[18:19], -1
	s_sleep 4
	s_cbranch_scc1 .LBB0_1438
	v_mov_b64_e32 v[0:1], s[8:9]
	flat_load_dword v0, v[0:1] sc1
	s_mov_b64 s[18:19], 0
	s_mov_b64 s[16:17], -1
	s_waitcnt vmcnt(0) lgkmcnt(0)
	v_cmp_eq_u32_e32 vcc, 0, v0
	s_and_saveexec_b64 s[20:21], vcc
	s_cmp_lt_u32 s25, 0x400001
	s_cselect_b64 s[18:19], -1, 0
	s_xor_b64 s[16:17], exec, -1
	s_and_b64 s[18:19], s[18:19], exec
	s_or_b64 exec, exec, s[20:21]
